# speedup vs baseline: 1.0130x; 1.0096x over previous
_Z7k_frontPKiS0_PKfPiP15HIP_vector_typeIjLj2EES2_S2_PDF16_S2_S7_:
	s_cmpk_gt_u32 s2, 0x186
	s_mov_b64 s[4:5], -1
	v_lshlrev_b32_e32 v1, 2, v0
	s_cbranch_scc0 .LBB0_4
	s_load_dwordx2 s[4:5], s[0:1], 0x28
	s_load_dwordx4 s[16:19], s[0:1], 0x40
	v_lshlrev_b32_e32 v30, 4, v0
	v_mov_b32_e32 v31, 0
	v_lshrrev_b32_e32 v33, 6, v0
	s_lshl_b32 s20, s2, 3
	s_addk_i32 s20, 0xf3c8
	s_movk_i32 s21, 0x186a
	s_movk_i32 s3, 0x110
	v_or_b32_e32 v2, s20, v33
	v_add_u32_e32 v53, 0x2000, v30
	v_add_u32_e32 v54, 0x4000, v30
	v_add_u32_e32 v55, 0x6000, v30
	v_cmp_gt_i32_e64 s[22:23], s21, v2
	s_waitcnt lgkmcnt(0)
	global_load_dwordx4 v[56:59], v30, s[4:5]
	global_load_dwordx4 v[60:63], v53, s[4:5]
	global_load_dwordx4 v[64:67], v54, s[4:5]
	global_load_dwordx4 v[68:71], v55, s[4:5]
	v_min_i32_e32 v2, 0x1869, v2
	v_lshlrev_b32_e32 v32, 4, v2
	v_bfe_u32 v40, v0, 5, 1
	v_and_b32_e32 v2, 31, v0
	v_or_b32_e32 v36, v32, v40
	v_lshlrev_b32_e32 v2, 4, v2
	v_mov_b32_e32 v3, v31
	v_ashrrev_i32_e32 v37, 31, v36
	s_waitcnt lgkmcnt(0)
	v_lshl_add_u64 v[34:35], s[16:17], 0, v[2:3]
	v_lshlrev_b64 v[2:3], 9, v[36:37]
	v_lshl_add_u64 v[10:11], v[34:35], 0, v[2:3]
	v_or_b32_e32 v2, 2, v36
	v_ashrrev_i32_e32 v3, 31, v2
	v_lshlrev_b64 v[2:3], 9, v[2:3]
	v_lshl_add_u64 v[12:13], v[34:35], 0, v[2:3]
	global_load_dwordx4 v[6:9], v[10:11], off nt
	global_load_dwordx4 v[2:5], v[12:13], off nt
	v_or_b32_e32 v10, 4, v36
	v_ashrrev_i32_e32 v11, 31, v10
	v_lshlrev_b64 v[10:11], 9, v[10:11]
	v_lshl_add_u64 v[18:19], v[34:35], 0, v[10:11]
	v_or_b32_e32 v10, 6, v36
	v_ashrrev_i32_e32 v11, 31, v10
	v_lshlrev_b64 v[10:11], 9, v[10:11]
	v_lshl_add_u64 v[20:21], v[34:35], 0, v[10:11]
	global_load_dwordx4 v[14:17], v[18:19], off nt
	global_load_dwordx4 v[10:13], v[20:21], off nt
	v_or_b32_e32 v18, 8, v36
	v_ashrrev_i32_e32 v19, 31, v18
	v_lshlrev_b64 v[18:19], 9, v[18:19]
	v_lshl_add_u64 v[26:27], v[34:35], 0, v[18:19]
	v_or_b32_e32 v18, 10, v36
	v_ashrrev_i32_e32 v19, 31, v18
	v_lshlrev_b64 v[18:19], 9, v[18:19]
	v_lshl_add_u64 v[28:29], v[34:35], 0, v[18:19]
	global_load_dwordx4 v[22:25], v[26:27], off nt
	global_load_dwordx4 v[18:21], v[28:29], off nt
	v_or_b32_e32 v26, 12, v36
	v_or_b32_e32 v36, 14, v36
	v_ashrrev_i32_e32 v27, 31, v26
	v_ashrrev_i32_e32 v37, 31, v36
	v_lshlrev_b64 v[26:27], 9, v[26:27]
	v_lshlrev_b64 v[36:37], 9, v[36:37]
	v_lshl_add_u64 v[26:27], v[34:35], 0, v[26:27]
	v_lshl_add_u64 v[34:35], v[34:35], 0, v[36:37]
	global_load_dwordx4 v[26:29], v[26:27], off nt
	v_and_b32_e32 v41, 0x7c, v1
	global_load_dwordx4 v[36:39], v[34:35], off nt
	v_and_b32_e32 v53, 15, v0
	v_mul_u32_u24_e32 v53, 0x440, v53
	v_lshrrev_b32_e32 v54, 4, v0
	v_lshl_add_u32 v53, v54, 1, v53
	s_waitcnt vmcnt(8)
	v_cvt_f16_f32_e32 v56, v56
	v_cvt_f16_f32_e32 v57, v57
	v_cvt_f16_f32_e32 v58, v58
	v_cvt_f16_f32_e32 v59, v59
	v_cvt_f16_f32_e32 v60, v60
	v_cvt_f16_f32_e32 v61, v61
	v_cvt_f16_f32_e32 v62, v62
	v_cvt_f16_f32_e32 v63, v63
	v_cvt_f16_f32_e32 v64, v64
	v_cvt_f16_f32_e32 v65, v65
	v_cvt_f16_f32_e32 v66, v66
	v_cvt_f16_f32_e32 v67, v67
	v_cvt_f16_f32_e32 v68, v68
	v_cvt_f16_f32_e32 v69, v69
	v_cvt_f16_f32_e32 v70, v70
	v_cvt_f16_f32_e32 v71, v71
	ds_write_b16 v53, v56
	ds_write_b16 v53, v57 offset:272
	ds_write_b16 v53, v58 offset:544
	ds_write_b16 v53, v59 offset:816
	ds_write_b16 v53, v60 offset:64
	ds_write_b16 v53, v61 offset:336
	ds_write_b16 v53, v62 offset:608
	ds_write_b16 v53, v63 offset:880
	ds_write_b16 v53, v64 offset:128
	ds_write_b16 v53, v65 offset:400
	ds_write_b16 v53, v66 offset:672
	ds_write_b16 v53, v67 offset:944
	ds_write_b16 v53, v68 offset:192
	ds_write_b16 v53, v69 offset:464
	ds_write_b16 v53, v70 offset:736
	ds_write_b16 v53, v71 offset:1008
	s_waitcnt lgkmcnt(0)
	s_barrier
	s_and_saveexec_b64 s[8:9], s[22:23]
	s_cbranch_execz .LBB0_3
	v_mul_u32_u24_e32 v34, 0x1100, v33
	v_lshrrev_b32_e32 v42, 1, v0
	v_lshl_or_b32 v41, v41, 1, v34
	v_and_b32_e32 v52, 24, v42
	v_and_b32_e32 v35, 15, v0
	v_mad_u32_u24 v40, v40, s3, v41
	v_lshlrev_b32_e32 v41, 1, v52
	v_add_u32_e32 v42, 0x4000, v40
	v_mad_u32_u24 v48, v35, s3, v41
	v_add_u32_e32 v43, 0x4800, v40
	v_add_u32_e32 v40, 0x5000, v40
	s_movk_i32 s4, 0x1100
	v_and_b32_e32 v30, 0x70, v30
	s_waitcnt vmcnt(7)
	v_cvt_pk_f16_f32 v9, v8, v9
	v_cvt_pk_f16_f32 v8, v6, v7
	s_waitcnt vmcnt(6)
	v_cvt_pk_f16_f32 v5, v4, v5
	v_cvt_pk_f16_f32 v4, v2, v3
	s_waitcnt vmcnt(5)
	v_cvt_pk_f16_f32 v3, v16, v17
	v_cvt_pk_f16_f32 v2, v14, v15
	s_waitcnt vmcnt(4)
	v_cvt_pk_f16_f32 v7, v12, v13
	v_cvt_pk_f16_f32 v6, v10, v11
	s_waitcnt vmcnt(3)
	v_cvt_pk_f16_f32 v11, v24, v25
	v_cvt_pk_f16_f32 v10, v22, v23
	s_waitcnt vmcnt(2)
	v_cvt_pk_f16_f32 v13, v20, v21
	v_cvt_pk_f16_f32 v12, v18, v19
	s_waitcnt vmcnt(1)
	v_cvt_pk_f16_f32 v15, v28, v29
	v_cvt_pk_f16_f32 v14, v26, v27
	s_waitcnt vmcnt(0)
	v_cvt_pk_f16_f32 v17, v38, v39
	v_cvt_pk_f16_f32 v16, v36, v37
	ds_write2_b64 v42, v[8:9], v[4:5] offset0:128 offset1:196
	ds_write2_b64 v43, v[2:3], v[6:7] offset0:8 offset1:76
	ds_write2_b64 v43, v[10:11], v[12:13] offset0:144 offset1:212
	ds_write2_b64 v40, v[14:15], v[16:17] offset0:24 offset1:92
	s_waitcnt lgkmcnt(0)
	ds_read_b128 v[2:5], v48
	v_mul_u32_u24_e32 v6, 0x110, v35
	v_mad_u32_u24 v33, v33, s4, v6
	v_add_u32_e32 v35, v33, v41
	ds_read_b128 v[6:9], v35 offset:17408
	ds_read_b128 v[10:13], v35 offset:17472
	ds_read_b128 v[14:17], v48 offset:64
	ds_read_b128 v[18:21], v48 offset:4352
	ds_read_b128 v[22:25], v48 offset:4416
	s_waitcnt lgkmcnt(4)
	v_mfma_f32_16x16x32_f16 v[2:5], v[2:5], v[6:9], 0
	ds_read_b128 v[26:29], v48 offset:8704
	ds_read_b128 v[36:39], v48 offset:8768
	ds_read_b128 v[40:43], v48 offset:13056
	ds_read_b128 v[44:47], v48 offset:13120
	s_waitcnt lgkmcnt(5)
	v_mfma_f32_16x16x32_f16 v[18:21], v[18:21], v[6:9], 0
	v_mfma_f32_16x16x32_f16 v[2:5], v[14:17], v[10:13], v[2:5]
	s_waitcnt lgkmcnt(4)
	v_mfma_f32_16x16x32_f16 v[14:17], v[22:25], v[10:13], v[18:21]
	ds_read_b128 v[22:25], v48 offset:128
	s_waitcnt lgkmcnt(4)
	v_mfma_f32_16x16x32_f16 v[26:29], v[26:29], v[6:9], 0
	s_waitcnt lgkmcnt(2)
	v_mfma_f32_16x16x32_f16 v[6:9], v[40:43], v[6:9], 0
	v_mfma_f32_16x16x32_f16 v[18:21], v[36:39], v[10:13], v[26:29]
	s_waitcnt lgkmcnt(1)
	v_mfma_f32_16x16x32_f16 v[6:9], v[44:47], v[10:13], v[6:9]
	ds_read_b128 v[10:13], v35 offset:17536
	s_nop 1
	ds_read_b128 v[26:29], v35 offset:17600
	ds_read_b128 v[36:39], v48 offset:192
	s_waitcnt lgkmcnt(2)
	v_mfma_f32_16x16x32_f16 v[2:5], v[22:25], v[10:13], v[2:5]
	ds_read_b128 v[22:25], v48 offset:4480
	ds_read_b128 v[40:43], v48 offset:4544
	s_waitcnt lgkmcnt(1)
	v_mfma_f32_16x16x32_f16 v[14:17], v[22:25], v[10:13], v[14:17]
	ds_read_b128 v[22:25], v48 offset:8832
	ds_read_b128 v[44:47], v48 offset:8896
	s_waitcnt lgkmcnt(1)
	v_mfma_f32_16x16x32_f16 v[18:21], v[22:25], v[10:13], v[18:21]
	ds_read_b128 v[22:25], v48 offset:13184
	ds_read_b128 v[48:51], v48 offset:13248
	s_waitcnt lgkmcnt(0)
	v_mfma_f32_16x16x32_f16 v[6:9], v[22:25], v[10:13], v[6:9]
	v_mfma_f32_16x16x32_f16 v[2:5], v[36:39], v[26:29], v[2:5]
	v_mfma_f32_16x16x32_f16 v[10:13], v[40:43], v[26:29], v[14:17]
	v_mfma_f32_16x16x32_f16 v[14:17], v[44:47], v[26:29], v[18:21]
	s_nop 5
	v_cvt_pk_f16_f32 v5, v4, v5
	v_cvt_pk_f16_f32 v4, v2, v3
	v_cvt_pk_f16_f32 v3, v12, v13
	v_mfma_f32_16x16x32_f16 v[6:9], v[48:51], v[26:29], v[6:9]
	v_add_u32_e32 v18, v33, v52
	v_cvt_pk_f16_f32 v2, v10, v11
	v_add_u32_e32 v10, 0x4000, v18
	ds_write2_b64 v10, v[4:5], v[2:3] offset0:128 offset1:132
	v_cvt_pk_f16_f32 v3, v16, v17
	v_cvt_pk_f16_f32 v2, v14, v15
	s_nop 1
	v_cvt_pk_f16_f32 v5, v8, v9
	v_cvt_pk_f16_f32 v4, v6, v7
	ds_write2_b64 v10, v[2:3], v[4:5] offset0:136 offset1:140
	v_bfe_u32 v6, v0, 3, 3
	v_or_b32_e32 v2, v34, v30
	v_mad_u32_u24 v8, v6, s3, v2
	s_waitcnt lgkmcnt(0)
	ds_read_b128 v[2:5], v8 offset:17408
	v_or_b32_e32 v12, v32, v6
	v_ashrrev_i32_e32 v13, 31, v12
	v_lshl_add_u64 v[10:11], s[18:19], 0, v[30:31]
	v_lshlrev_b64 v[6:7], 7, v[12:13]
	v_lshl_add_u64 v[14:15], v[10:11], 0, v[6:7]
	ds_read_b128 v[6:9], v8 offset:19584
	s_waitcnt lgkmcnt(1)
	global_store_dwordx4 v[14:15], v[2:5], off sc1
	s_nop 1
	v_or_b32_e32 v2, 8, v12
	v_ashrrev_i32_e32 v3, 31, v2
	v_lshlrev_b64 v[2:3], 7, v[2:3]
	v_lshl_add_u64 v[2:3], v[10:11], 0, v[2:3]
	s_waitcnt lgkmcnt(0)
	global_store_dwordx4 v[2:3], v[6:9], off sc1

.LBB0_35:
	s_or_b64 exec, exec, s[6:7]
	v_lshlrev_b32_e32 v1, 3, v0
	s_waitcnt lgkmcnt(0)
	s_barrier
	ds_read_b64 v[4:5], v1 offset:8192
	ds_read_b64 v[6:7], v1 offset:12288
	ds_read_b64 v[8:9], v1 offset:16384
	ds_read_b64 v[10:11], v1 offset:20480
	ds_read_b64 v[12:13], v1 offset:24576
	ds_read_b64 v[14:15], v1 offset:28672
	ds_read_b64 v[16:17], v1 offset:32768
	ds_read_b64 v[18:19], v1 offset:36864
	v_add_u32_e32 v2, s10, v0
	v_lshlrev_b32_e32 v2, 3, v2
	v_add_u32_e32 v20, 0x1000, v2
	v_add_u32_e32 v21, 0x2000, v2
	v_add_u32_e32 v22, 0x3000, v2
	v_add_u32_e32 v23, 0x4000, v2
	v_add_u32_e32 v24, 0x5000, v2
	v_add_u32_e32 v25, 0x6000, v2
	v_add_u32_e32 v26, 0x7000, v2
	s_waitcnt lgkmcnt(7)
	global_store_dwordx2 v2, v[4:5], s[4:5] sc1
	s_mov_b64 s[6:7], exec
	v_or_b32_e32 v3, 0x200, v0
	v_cmp_gt_u32_e32 vcc, s3, v3
	s_and_b64 exec, exec, vcc
	s_cbranch_execz .LBB0_43
	s_waitcnt lgkmcnt(6)
	global_store_dwordx2 v20, v[6:7], s[4:5] sc1
	v_or_b32_e32 v3, 0x400, v0
	v_cmp_gt_u32_e32 vcc, s3, v3
	s_and_b64 exec, exec, vcc
	s_cbranch_execz .LBB0_43
	s_waitcnt lgkmcnt(5)
	global_store_dwordx2 v21, v[8:9], s[4:5] sc1
	v_or_b32_e32 v3, 0x600, v0
	v_cmp_gt_u32_e32 vcc, s3, v3
	s_and_b64 exec, exec, vcc
	s_cbranch_execz .LBB0_43
	s_waitcnt lgkmcnt(4)
	global_store_dwordx2 v22, v[10:11], s[4:5] sc1
	v_or_b32_e32 v3, 0x800, v0
	v_cmp_gt_u32_e32 vcc, s3, v3
	s_and_b64 exec, exec, vcc
	s_cbranch_execz .LBB0_43
	s_waitcnt lgkmcnt(3)
	global_store_dwordx2 v23, v[12:13], s[4:5] sc1
	v_or_b32_e32 v3, 0xa00, v0
	v_cmp_gt_u32_e32 vcc, s3, v3
	s_and_b64 exec, exec, vcc
	s_cbranch_execz .LBB0_43
	s_waitcnt lgkmcnt(2)
	global_store_dwordx2 v24, v[14:15], s[4:5] sc1
	v_or_b32_e32 v3, 0xc00, v0
	v_cmp_gt_u32_e32 vcc, s3, v3
	s_and_b64 exec, exec, vcc
	s_cbranch_execz .LBB0_43
	s_waitcnt lgkmcnt(1)
	global_store_dwordx2 v25, v[16:17], s[4:5] sc1
	v_or_b32_e32 v3, 0xe00, v0
	v_cmp_gt_u32_e32 vcc, s3, v3
	s_and_b64 exec, exec, vcc
	s_cbranch_execz .LBB0_43
	s_waitcnt lgkmcnt(0)
	global_store_dwordx2 v26, v[18:19], s[4:5] sc1

.LBB1_89:
	ds_read2st64_b64 v[10:13], v7 offset1:8
	ds_read2st64_b64 v[14:17], v7 offset0:16 offset1:24
	ds_read2st64_b64 v[18:21], v7 offset0:32 offset1:40
	ds_read2st64_b64 v[24:27], v7 offset0:48 offset1:56
	v_add_u32_e32 v28, s34, v2
	s_waitcnt lgkmcnt(3)
	v_cvt_pk_f16_f32 v1, v11, v13
	s_waitcnt lgkmcnt(2)
	v_cvt_pk_f16_f32 v9, v15, v17
	s_waitcnt lgkmcnt(1)
	v_cvt_pk_f16_f32 v11, v19, v21
	s_waitcnt lgkmcnt(0)
	v_cvt_pk_f16_f32 v13, v25, v27
	v_lshlrev_b32_e32 v15, 16, v1
	v_add_u32_e32 v6, -4, v6
	v_and_b32_e32 v1, 0xffff0000, v1
	v_lshlrev_b32_e32 v17, 16, v9
	v_and_b32_e32 v9, 0xffff0000, v9
	v_lshlrev_b32_e32 v19, 16, v11
	v_and_b32_e32 v11, 0xffff0000, v11
	v_lshlrev_b32_e32 v21, 16, v13
	v_and_b32_e32 v13, 0xffff0000, v13
	v_add_u32_e32 v15, 0x10000, v15
	v_add_u32_e32 v30, s34, v3
	v_add_u32_e32 v32, s16, v2
	v_add_u32_e32 v34, s17, v3
	v_add_u32_e32 v36, s18, v2
	v_add_u32_e32 v38, s19, v3
	v_add_u32_e32 v40, s20, v2
	v_add_u32_e32 v42, s21, v3
	s_add_i32 s15, s15, 8
	v_ashrrev_i32_e32 v29, 31, v28
	v_cmp_eq_u32_e32 vcc, 0, v6
	v_add_u32_e32 v1, 0x10000, v1
	v_add_u32_e32 v9, 0x10000, v9
	v_add_u32_e32 v17, 0x10000, v17
	v_add_u32_e32 v11, 0x10000, v11
	v_add_u32_e32 v19, 0x10000, v19
	v_add_u32_e32 v13, 0x10000, v13
	v_add_u32_e32 v21, 0x10000, v21
	v_and_b32_e32 v15, 0xfffe0000, v15
	v_add_u32_e32 v3, 0x1000, v3
	v_add_u32_e32 v2, 0x1000, v2
	v_add_u32_e32 v7, 0x8000, v7
	v_ashrrev_i32_e32 v31, 31, v30
	v_ashrrev_i32_e32 v35, 31, v34
	v_ashrrev_i32_e32 v33, 31, v32
	v_ashrrev_i32_e32 v39, 31, v38
	v_ashrrev_i32_e32 v37, 31, v36
	v_ashrrev_i32_e32 v43, 31, v42
	v_ashrrev_i32_e32 v41, 31, v40
	v_mov_b32_e32 v8, s15
	v_lshl_add_u64 v[28:29], v[28:29], 2, s[24:25]
	s_or_b64 s[12:13], vcc, s[12:13]
	v_and_b32_e32 v1, 0xfffe0000, v1
	v_and_b32_e32 v9, 0xfffe0000, v9
	v_and_b32_e32 v17, 0xfffe0000, v17
	v_and_b32_e32 v11, 0xfffe0000, v11
	v_and_b32_e32 v19, 0xfffe0000, v19
	v_and_b32_e32 v13, 0xfffe0000, v13
	v_and_b32_e32 v21, 0xfffe0000, v21
	v_or_b32_e32 v10, v15, v10
	v_lshl_add_u64 v[30:31], v[30:31], 2, s[24:25]
	v_lshl_add_u64 v[32:33], v[32:33], 2, s[24:25]
	v_lshl_add_u64 v[34:35], v[34:35], 2, s[24:25]
	v_lshl_add_u64 v[36:37], v[36:37], 2, s[24:25]
	v_lshl_add_u64 v[38:39], v[38:39], 2, s[24:25]
	v_lshl_add_u64 v[40:41], v[40:41], 2, s[24:25]
	v_lshl_add_u64 v[42:43], v[42:43], 2, s[24:25]
	v_or_b32_e32 v1, v1, v12
	v_or_b32_e32 v9, v9, v16
	v_or_b32_e32 v12, v17, v14
	v_or_b32_e32 v11, v11, v20
	v_or_b32_e32 v14, v19, v18
	v_or_b32_e32 v13, v13, v26
	v_or_b32_e32 v15, v21, v24
	global_store_dword v[28:29], v10, off sc1
	global_store_dword v[30:31], v1, off sc1
	global_store_dword v[32:33], v12, off sc1
	global_store_dword v[34:35], v9, off sc1
	global_store_dword v[36:37], v14, off sc1
	global_store_dword v[38:39], v11, off sc1
	global_store_dword v[40:41], v15, off sc1
	global_store_dword v[42:43], v13, off sc1
	s_andn2_b64 exec, exec, s[12:13]
	s_cbranch_execnz .LBB1_89
	s_or_b64 exec, exec, s[12:13]

.LBB1_93:
	ds_read2st64_b64 v[6:9], v5 offset1:8
	v_add_u32_e32 v10, s34, v2
	v_add_u32_e32 v1, -1, v1
	v_add_u32_e32 v12, s34, v3
	v_ashrrev_i32_e32 v11, 31, v10
	s_waitcnt lgkmcnt(0)
	v_cvt_pk_f16_f32 v7, v7, v9
	v_lshlrev_b32_e32 v9, 16, v7
	v_and_b32_e32 v7, 0xffff0000, v7
	v_add_u32_e32 v9, 0x10000, v9
	v_cmp_eq_u32_e32 vcc, 0, v1
	v_add_u32_e32 v7, 0x10000, v7
	v_and_b32_e32 v9, 0xfffe0000, v9
	v_add_u32_e32 v3, 0x400, v3
	v_add_u32_e32 v2, 0x400, v2
	v_add_u32_e32 v5, 0x2000, v5
	v_ashrrev_i32_e32 v13, 31, v12
	v_lshl_add_u64 v[10:11], v[10:11], 2, s[24:25]
	s_or_b64 s[12:13], vcc, s[12:13]
	v_and_b32_e32 v7, 0xfffe0000, v7
	v_or_b32_e32 v6, v9, v6
	v_lshl_add_u64 v[12:13], v[12:13], 2, s[24:25]
	v_or_b32_e32 v7, v7, v8
	global_store_dword v[10:11], v6, off sc1
	global_store_dword v[12:13], v7, off sc1
	s_andn2_b64 exec, exec, s[12:13]
	s_cbranch_execnz .LBB1_93

.LBB1_98:
	ds_read_b64 v[6:7], v4
	v_ashrrev_i32_e32 v3, 31, v2
	v_lshl_add_u64 v[8:9], v[2:3], 2, s[24:25]
	v_add_u32_e32 v1, 0x200, v1
	v_cmp_le_i32_e32 vcc, s33, v1
	s_waitcnt lgkmcnt(0)
	v_cvt_f16_f32_sdwa v3, v7 dst_sel:WORD_1 dst_unused:UNUSED_PAD src0_sel:DWORD
	v_add_u32_e32 v4, 0x1000, v4
	v_add_u32_e32 v2, 0x200, v2
	s_or_b64 s[4:5], vcc, s[4:5]
	v_add_u32_e32 v3, 0x10000, v3
	v_and_or_b32 v3, v3, s6, v6
	global_store_dword v[8:9], v3, off sc1
	s_andn2_b64 exec, exec, s[4:5]
	s_cbranch_execnz .LBB1_98

.LBB1_100:
	v_lshrrev_b32_e32 v20, 3, v0
	v_and_b32_e32 v1, 7, v0
	v_lshlrev_b32_e32 v1, 4, v1
	v_or_b32_e32 v24, s46, v20
	v_lshlrev_b32_e32 v20, 2, v20
	s_mov_b32 s2, 0x186a0
	s_waitcnt lgkmcnt(0)
	s_barrier
	ds_read_b32 v26, v20 offset:4220
	ds_read_b32 v28, v20 offset:4476
	ds_read_b32 v30, v20 offset:4732
	ds_read_b32 v32, v20 offset:4988
	v_cvt_f32_f16_e32 v2, v60
	v_cvt_f32_f16_sdwa v3, v60 dst_sel:DWORD dst_unused:UNUSED_PAD src0_sel:WORD_1
	v_cvt_f32_f16_e32 v4, v61
	v_cvt_f32_f16_sdwa v5, v61 dst_sel:DWORD dst_unused:UNUSED_PAD src0_sel:WORD_1
	v_cvt_f32_f16_e32 v6, v62
	v_cvt_f32_f16_sdwa v7, v62 dst_sel:DWORD dst_unused:UNUSED_PAD src0_sel:WORD_1
	v_cvt_f32_f16_e32 v8, v63
	v_cvt_f32_f16_sdwa v9, v63 dst_sel:DWORD dst_unused:UNUSED_PAD src0_sel:WORD_1
	v_add_u32_e32 v10, 0, v24
	s_waitcnt lgkmcnt(3)
	v_pk_mul_f32 v[2:3], v[26:27], v[2:3] op_sel_hi:[0,1]
	v_pk_mul_f32 v[4:5], v[26:27], v[4:5] op_sel_hi:[0,1]
	v_pk_mul_f32 v[6:7], v[26:27], v[6:7] op_sel_hi:[0,1]
	v_pk_mul_f32 v[8:9], v[26:27], v[8:9] op_sel_hi:[0,1]
	v_cmp_gt_u32_e32 vcc, s2, v10
	v_lshl_or_b32 v11, v10, 7, v1
	v_cvt_pk_f16_f32 v60, v2, v3
	v_cvt_pk_f16_f32 v61, v4, v5
	v_cvt_pk_f16_f32 v62, v6, v7
	v_cvt_pk_f16_f32 v63, v8, v9
	s_and_saveexec_b64 s[0:1], vcc
	global_store_dwordx4 v11, v[60:63], s[44:45] sc1
	s_or_b64 exec, exec, s[0:1]
	v_cvt_f32_f16_e32 v2, v64
	v_cvt_f32_f16_sdwa v3, v64 dst_sel:DWORD dst_unused:UNUSED_PAD src0_sel:WORD_1
	v_cvt_f32_f16_e32 v4, v65
	v_cvt_f32_f16_sdwa v5, v65 dst_sel:DWORD dst_unused:UNUSED_PAD src0_sel:WORD_1
	v_cvt_f32_f16_e32 v6, v66
	v_cvt_f32_f16_sdwa v7, v66 dst_sel:DWORD dst_unused:UNUSED_PAD src0_sel:WORD_1
	v_cvt_f32_f16_e32 v8, v67
	v_cvt_f32_f16_sdwa v9, v67 dst_sel:DWORD dst_unused:UNUSED_PAD src0_sel:WORD_1
	v_add_u32_e32 v10, 64, v24
	s_waitcnt lgkmcnt(2)
	v_pk_mul_f32 v[2:3], v[28:29], v[2:3] op_sel_hi:[0,1]
	v_pk_mul_f32 v[4:5], v[28:29], v[4:5] op_sel_hi:[0,1]
	v_pk_mul_f32 v[6:7], v[28:29], v[6:7] op_sel_hi:[0,1]
	v_pk_mul_f32 v[8:9], v[28:29], v[8:9] op_sel_hi:[0,1]
	v_cmp_gt_u32_e32 vcc, s2, v10
	v_lshl_or_b32 v11, v10, 7, v1
	v_cvt_pk_f16_f32 v64, v2, v3
	v_cvt_pk_f16_f32 v65, v4, v5
	v_cvt_pk_f16_f32 v66, v6, v7
	v_cvt_pk_f16_f32 v67, v8, v9
	s_and_saveexec_b64 s[0:1], vcc
	global_store_dwordx4 v11, v[64:67], s[44:45] sc1
	s_or_b64 exec, exec, s[0:1]
	v_cvt_f32_f16_e32 v2, v68
	v_cvt_f32_f16_sdwa v3, v68 dst_sel:DWORD dst_unused:UNUSED_PAD src0_sel:WORD_1
	v_cvt_f32_f16_e32 v4, v69
	v_cvt_f32_f16_sdwa v5, v69 dst_sel:DWORD dst_unused:UNUSED_PAD src0_sel:WORD_1
	v_cvt_f32_f16_e32 v6, v70
	v_cvt_f32_f16_sdwa v7, v70 dst_sel:DWORD dst_unused:UNUSED_PAD src0_sel:WORD_1
	v_cvt_f32_f16_e32 v8, v71
	v_cvt_f32_f16_sdwa v9, v71 dst_sel:DWORD dst_unused:UNUSED_PAD src0_sel:WORD_1
	v_add_u32_e32 v10, 0x80, v24
	s_waitcnt lgkmcnt(1)
	v_pk_mul_f32 v[2:3], v[30:31], v[2:3] op_sel_hi:[0,1]
	v_pk_mul_f32 v[4:5], v[30:31], v[4:5] op_sel_hi:[0,1]
	v_pk_mul_f32 v[6:7], v[30:31], v[6:7] op_sel_hi:[0,1]
	v_pk_mul_f32 v[8:9], v[30:31], v[8:9] op_sel_hi:[0,1]
	v_cmp_gt_u32_e32 vcc, s2, v10
	v_lshl_or_b32 v11, v10, 7, v1
	v_cvt_pk_f16_f32 v68, v2, v3
	v_cvt_pk_f16_f32 v69, v4, v5
	v_cvt_pk_f16_f32 v70, v6, v7
	v_cvt_pk_f16_f32 v71, v8, v9
	s_and_saveexec_b64 s[0:1], vcc
	global_store_dwordx4 v11, v[68:71], s[44:45] sc1
	s_or_b64 exec, exec, s[0:1]
	v_cvt_f32_f16_e32 v2, v56
	v_cvt_f32_f16_sdwa v3, v56 dst_sel:DWORD dst_unused:UNUSED_PAD src0_sel:WORD_1
	v_cvt_f32_f16_e32 v4, v57
	v_cvt_f32_f16_sdwa v5, v57 dst_sel:DWORD dst_unused:UNUSED_PAD src0_sel:WORD_1
	v_cvt_f32_f16_e32 v6, v58
	v_cvt_f32_f16_sdwa v7, v58 dst_sel:DWORD dst_unused:UNUSED_PAD src0_sel:WORD_1
	v_cvt_f32_f16_e32 v8, v59
	v_cvt_f32_f16_sdwa v9, v59 dst_sel:DWORD dst_unused:UNUSED_PAD src0_sel:WORD_1
	v_add_u32_e32 v10, 0xc0, v24
	s_waitcnt lgkmcnt(0)
	v_pk_mul_f32 v[2:3], v[32:33], v[2:3] op_sel_hi:[0,1]
	v_pk_mul_f32 v[4:5], v[32:33], v[4:5] op_sel_hi:[0,1]
	v_pk_mul_f32 v[6:7], v[32:33], v[6:7] op_sel_hi:[0,1]
	v_pk_mul_f32 v[8:9], v[32:33], v[8:9] op_sel_hi:[0,1]
	v_cmp_gt_u32_e32 vcc, s2, v10
	v_lshl_or_b32 v11, v10, 7, v1
	v_cvt_pk_f16_f32 v56, v2, v3
	v_cvt_pk_f16_f32 v57, v4, v5
	v_cvt_pk_f16_f32 v58, v6, v7
	v_cvt_pk_f16_f32 v59, v8, v9
	s_and_saveexec_b64 s[0:1], vcc
	global_store_dwordx4 v11, v[56:59], s[44:45] sc1
	s_or_b64 exec, exec, s[0:1]
	s_endpgm

.LBB2_6:
	s_or_b64 exec, exec, s[6:7]
	v_and_b32_e32 v13, 15, v0
	v_lshlrev_b32_e32 v15, 4, v1
	v_lshlrev_b32_e32 v2, 5, v17
	v_lshrrev_b32_e32 v0, 1, v0
	v_or_b32_e32 v1, v15, v13
	s_waitcnt lgkmcnt(0)
	global_load_dwordx4 v[28:31], v2, s[2:3]
	global_load_dwordx4 v[32:35], v2, s[2:3] offset:16
	v_mov_b32_e32 v9, 0
	v_and_b32_e32 v11, 24, v0
	s_waitcnt vmcnt(3)
	v_lshlrev_b32_e32 v8, 7, v1
	v_lshl_add_u64 v[0:1], s[8:9], 0, v[8:9]
	v_lshlrev_b32_e32 v8, 1, v11
	v_lshl_add_u64 v[36:37], v[0:1], 0, v[8:9]
	global_load_dwordx4 v[4:7], v[36:37], off
	global_load_dwordx4 v[0:3], v[36:37], off offset:64
	s_movk_i32 s2, 0x90
	v_lshlrev_b32_e32 v12, 3, v17
	v_mad_u32_u24 v10, v16, s2, v10
	v_cmp_eq_u32_e32 vcc, 0, v17
	s_waitcnt vmcnt(3)
	v_fma_f32 v19, v18, v19, v28
	v_fma_f32 v20, v18, v20, v29
	v_fma_f32 v21, v18, v21, v30
	v_fmac_f32_e32 v31, v18, v22
	s_waitcnt vmcnt(2)
	v_fma_f32 v22, v18, v23, v32
	v_fma_f32 v23, v18, v24, v33
	v_fma_f32 v24, v18, v25, v34
	v_fmac_f32_e32 v35, v18, v26
	v_max_f32_e32 v19, 0, v19
	v_max_f32_e32 v20, 0, v20
	v_max_f32_e32 v21, 0, v21
	v_max_f32_e32 v25, 0, v31
	v_max_f32_e32 v22, 0, v22
	v_max_f32_e32 v26, 0, v23
	v_max_f32_e32 v23, 0, v24
	v_max_f32_e32 v24, 0, v35
	v_cvt_pk_f16_f32 v23, v23, v24
	v_cvt_pk_f16_f32 v22, v22, v26
	v_cvt_pk_f16_f32 v21, v21, v25
	v_cvt_pk_f16_f32 v20, v19, v20
	ds_write_b128 v10, v[20:23] offset:4608
	s_and_saveexec_b64 s[0:1], vcc
	v_lshlrev_b32_e32 v10, 2, v16
	ds_write_b32 v10, v18 offset:9216
	s_or_b64 exec, exec, s[0:1]
	v_mad_u32_u24 v8, v13, s2, v8
	s_waitcnt lgkmcnt(0)
	s_barrier
	ds_read_b128 v[16:19], v8 offset:4608
	ds_read_b128 v[20:23], v8 offset:4672
	s_waitcnt vmcnt(1) lgkmcnt(1)
	v_mfma_f32_16x16x32_f16 a[0:3], v[4:7], v[16:19], 0
	v_lshlrev_b32_e32 v10, 1, v15
	v_mul_u32_u24_e32 v15, 0x90, v13
	v_lshlrev_b32_e32 v13, 2, v13
	v_add_u32_e32 v13, 0x2400, v13
	ds_read2_b32 v[24:25], v13 offset1:16
	s_waitcnt vmcnt(0) lgkmcnt(1)
	v_mfma_f32_16x16x32_f16 a[0:3], v[0:3], v[20:23], a[0:3]
	ds_read_b128 v[20:23], v8 offset:6976
	s_nop 6
	v_accvgpr_read_b32 v17, a2
	v_accvgpr_read_b32 v16, a1
	s_waitcnt lgkmcnt(1)
	v_pk_mul_f32 v[16:17], v[24:25], v[16:17] op_sel_hi:[0,1]
	v_cvt_pk_f16_f32 v27, v16, v17
	ds_read_b128 v[16:19], v8 offset:6912
	v_accvgpr_read_b32 v13, a0
	v_fma_mixlo_f16 v13, v24, v13, 0
	v_pack_b32_f16 v26, v13, v27
	v_accvgpr_read_b32 v13, a3
	s_waitcnt lgkmcnt(0)
	v_mfma_f32_16x16x32_f16 a[0:3], v[4:7], v[16:19], 0
	v_fma_mixlo_f16 v13, v24, v13, 0
	v_add3_u32 v4, v10, v11, v15
	v_alignbit_b32 v27, v13, v27, 16
	v_mfma_f32_16x16x32_f16 a[0:3], v[0:3], v[20:23], a[0:3]
	ds_write_b64 v4, v[26:27]
	v_add_u32_e32 v8, s12, v14
	s_nop 5
	v_accvgpr_read_b32 v0, a0
	v_fma_mixlo_f16 v5, v25, v0, 0
	v_mov_b32_e32 v0, v25
	v_accvgpr_read_b32 v3, a2
	v_accvgpr_read_b32 v2, a1
	v_pk_mul_f32 v[0:1], v[0:1], v[2:3] op_sel_hi:[0,1]
	v_accvgpr_read_b32 v2, a3
	v_cvt_pk_f16_f32 v1, v0, v1
	v_fma_mixlo_f16 v2, v25, v2, 0
	v_pack_b32_f16 v0, v5, v1
	v_alignbit_b32 v1, v2, v1, 16
	ds_write_b64 v4, v[0:1] offset:2304
	v_mad_u32_u24 v0, v14, s2, v12
	s_waitcnt lgkmcnt(0)
	s_barrier
	ds_read2_b64 v[2:5], v0 offset1:8
	v_lshlrev_b64 v[0:1], 7, v[8:9]
	v_lshl_add_u64 v[0:1], s[10:11], 0, v[0:1]
	v_lshlrev_b32_e32 v8, 1, v12
	v_lshl_add_u64 v[0:1], v[0:1], 0, v[8:9]
	s_waitcnt lgkmcnt(0)
	global_store_dwordx4 v[0:1], v[2:5], off sc1 nt
	s_endpgm
	.p2alignl 8, 3212836864

.LBB3_6:
	s_or_b64 exec, exec, s[8:9]
	s_waitcnt lgkmcnt(0)
	global_load_dwordx4 v[0:3], v8, s[2:3]
	global_load_dwordx4 v[18:21], v8, s[2:3] offset:128
	v_lshlrev_b64 v[4:5], 8, v[4:5]
	v_mov_b32_e32 v9, 0
	v_lshl_add_u64 v[4:5], s[6:7], 0, v[4:5]
	v_lshl_add_u64 v[8:9], v[4:5], 0, v[8:9]
	s_waitcnt vmcnt(1)
	v_pk_fma_f32 v[0:1], v[6:7], v[16:17], v[0:1] op_sel_hi:[0,1,1]
	v_pk_fma_f32 v[2:3], v[6:7], v[14:15], v[2:3] op_sel_hi:[0,1,1]
	s_waitcnt vmcnt(0)
	v_pk_fma_f32 v[4:5], v[6:7], v[12:13], v[18:19] op_sel_hi:[0,1,1]
	v_pk_fma_f32 v[6:7], v[6:7], v[10:11], v[20:21] op_sel_hi:[0,1,1]
	global_store_dwordx4 v[8:9], v[0:3], off sc1 nt
	global_store_dwordx4 v[8:9], v[4:7], off offset:128 sc1 nt
	s_endpgm
	.p2alignl 8, 3212836864
